# v70 + phase F residual epilogue: second half-tile's residual rows requested during the first half; NSA top-8 rank-count loops: eight LDS reads per iteration issued together with counted waits
# baseline (speedup 1.0000x reference)
.LBB0_3704:
	v_add_u32_e32 v71, s0, v68
	ds_read2_b32 v[198:199], v71 offset1:1
	ds_read2_b32 v[200:201], v71 offset0:2 offset1:3
	ds_read2_b32 v[202:203], v71 offset0:4 offset1:5
	ds_read2_b32 v[204:205], v71 offset0:6 offset1:7
	ds_read2_b32 v[206:207], v71 offset0:8 offset1:9
	ds_read2_b32 v[208:209], v71 offset0:10 offset1:11
	ds_read2_b32 v[210:211], v71 offset0:12 offset1:13
	ds_read2_b32 v[212:213], v71 offset0:14 offset1:15
	v_cmp_lt_u32_e64 s[12:13], s3, v84
	v_cmp_lt_u32_e64 s[14:15], s2, v67
	s_add_i32 s0, s0, 64
	s_waitcnt lgkmcnt(7)
	v_cmp_gt_f32_e32 vcc, v199, v69
	v_cmp_gt_f32_e64 s[6:7], v198, v66
	v_cmp_eq_f32_e64 s[8:9], v198, v66
	v_cmp_eq_f32_e64 s[10:11], v199, v69
	s_and_b64 s[10:11], s[10:11], s[14:15]
	s_and_b64 s[8:9], s[8:9], s[12:13]
	s_or_b64 s[6:7], s[6:7], s[8:9]
	s_or_b64 s[8:9], vcc, s[10:11]
	s_add_i32 s14, s3, 2
	s_add_i32 s12, s2, 2
	v_cndmask_b32_e64 v75, 0, 1, s[8:9]
	s_waitcnt lgkmcnt(6)
	v_cmp_eq_f32_e64 s[8:9], v201, v69
	v_cmp_eq_f32_e64 s[10:11], v200, v66
	v_cmp_lt_u32_e64 s[12:13], s12, v67
	v_cmp_lt_u32_e64 s[14:15], s14, v84
	v_cndmask_b32_e64 v78, 0, 1, s[6:7]
	v_cmp_gt_f32_e32 vcc, v200, v66
	v_cmp_gt_f32_e64 s[6:7], v201, v69
	s_and_b64 s[10:11], s[10:11], s[14:15]
	s_and_b64 s[8:9], s[8:9], s[12:13]
	s_or_b64 s[6:7], s[6:7], s[8:9]
	s_or_b64 vcc, vcc, s[10:11]
	v_addc_co_u32_e32 v76, vcc, v74, v78, vcc
	v_addc_co_u32_e64 v73, vcc, v73, v75, s[6:7]
	s_add_i32 s14, s3, 4
	s_add_i32 s12, s2, 4
	v_cmp_lt_u32_e64 s[12:13], s12, v67
	v_cmp_lt_u32_e64 s[14:15], s14, v84
	s_waitcnt lgkmcnt(5)
	v_cmp_gt_f32_e32 vcc, v202, v66
	v_cmp_gt_f32_e64 s[6:7], v203, v69
	v_cmp_eq_f32_e64 s[8:9], v203, v69
	v_cmp_eq_f32_e64 s[10:11], v202, v66
	s_and_b64 s[10:11], s[10:11], s[14:15]
	s_and_b64 s[8:9], s[8:9], s[12:13]
	s_or_b64 s[6:7], s[6:7], s[8:9]
	s_or_b64 s[8:9], vcc, s[10:11]
	v_cndmask_b32_e64 v77, 0, 1, s[8:9]
	v_cndmask_b32_e64 v78, 0, 1, s[6:7]
	s_add_i32 s14, s2, 6
	s_add_i32 s12, s3, 6
	s_waitcnt lgkmcnt(4)
	v_cmp_gt_f32_e32 vcc, v205, v69
	v_cmp_gt_f32_e64 s[6:7], v204, v66
	v_cmp_eq_f32_e64 s[8:9], v204, v66
	v_cmp_eq_f32_e64 s[10:11], v205, v69
	v_cmp_lt_u32_e64 s[12:13], s12, v84
	v_cmp_lt_u32_e64 s[14:15], s14, v67
	s_and_b64 s[10:11], s[10:11], s[14:15]
	s_and_b64 s[8:9], s[8:9], s[12:13]
	s_or_b64 s[6:7], s[6:7], s[8:9]
	s_or_b64 vcc, vcc, s[10:11]
	v_addc_co_u32_e32 v73, vcc, v73, v78, vcc
	v_addc_co_u32_e64 v76, vcc, v76, v77, s[6:7]
	s_waitcnt lgkmcnt(3)
	v_cmp_gt_f32_e32 vcc, v207, v69
	v_cmp_gt_f32_e64 s[6:7], v206, v66
	v_cmp_eq_f32_e64 s[8:9], v206, v66
	v_cmp_eq_f32_e64 s[10:11], v207, v69
	s_add_i32 s14, s2, 8
	s_add_i32 s12, s3, 8
	v_cmp_lt_u32_e64 s[12:13], s12, v84
	v_cmp_lt_u32_e64 s[14:15], s14, v67
	s_and_b64 s[10:11], s[10:11], s[14:15]
	s_and_b64 s[8:9], s[8:9], s[12:13]
	s_or_b64 s[6:7], s[6:7], s[8:9]
	s_or_b64 s[8:9], vcc, s[10:11]
	v_cndmask_b32_e64 v77, 0, 1, s[8:9]
	v_cndmask_b32_e64 v78, 0, 1, s[6:7]
	s_add_i32 s14, s3, 10
	s_add_i32 s12, s2, 10
	s_waitcnt lgkmcnt(2)
	v_cmp_gt_f32_e32 vcc, v208, v66
	v_cmp_gt_f32_e64 s[6:7], v209, v69
	v_cmp_eq_f32_e64 s[8:9], v209, v69
	v_cmp_eq_f32_e64 s[10:11], v208, v66
	v_cmp_lt_u32_e64 s[12:13], s12, v67
	v_cmp_lt_u32_e64 s[14:15], s14, v84
	s_and_b64 s[10:11], s[10:11], s[14:15]
	s_and_b64 s[8:9], s[8:9], s[12:13]
	s_or_b64 s[6:7], s[6:7], s[8:9]
	s_or_b64 vcc, vcc, s[10:11]
	v_addc_co_u32_e32 v76, vcc, v76, v78, vcc
	v_addc_co_u32_e64 v73, vcc, v73, v77, s[6:7]
	s_waitcnt lgkmcnt(1)
	v_cmp_gt_f32_e32 vcc, v210, v66
	v_cmp_gt_f32_e64 s[6:7], v211, v69
	v_cmp_eq_f32_e64 s[8:9], v211, v69
	v_cmp_eq_f32_e64 s[10:11], v210, v66
	s_add_i32 s14, s3, 12
	s_add_i32 s12, s2, 12
	v_cmp_lt_u32_e64 s[12:13], s12, v67
	v_cmp_lt_u32_e64 s[14:15], s14, v84
	s_and_b64 s[10:11], s[10:11], s[14:15]
	s_and_b64 s[8:9], s[8:9], s[12:13]
	s_or_b64 s[6:7], s[6:7], s[8:9]
	s_or_b64 s[8:9], vcc, s[10:11]
	s_add_i32 s14, s2, 14
	s_add_i32 s12, s3, 14
	v_cndmask_b32_e64 v77, 0, 1, s[8:9]
	s_waitcnt lgkmcnt(0)
	v_cmp_eq_f32_e64 s[8:9], v212, v66
	v_cmp_eq_f32_e64 s[10:11], v213, v69
	v_cmp_lt_u32_e64 s[12:13], s12, v84
	v_cmp_lt_u32_e64 s[14:15], s14, v67
	v_cndmask_b32_e64 v78, 0, 1, s[6:7]
	v_cmp_gt_f32_e32 vcc, v213, v69
	v_cmp_gt_f32_e64 s[6:7], v212, v66
	s_and_b64 s[10:11], s[10:11], s[14:15]
	s_and_b64 s[8:9], s[8:9], s[12:13]
	s_or_b64 s[6:7], s[6:7], s[8:9]
	s_or_b64 vcc, vcc, s[10:11]
	s_add_i32 s3, s3, 16
	s_add_i32 s2, s2, 16
	v_addc_co_u32_e32 v73, vcc, v73, v78, vcc
	v_addc_co_u32_e64 v74, vcc, v76, v77, s[6:7]
	s_cmpk_lg_i32 s0, 0x80
	s_cbranch_scc1 .LBB0_3704
	v_add_u32_e32 v66, v74, v73
	v_and_b32_e32 v71, 32, v154
	v_cmp_eq_u32_e32 vcc, 0, v84
	v_cmp_gt_u32_e64 s[6:7], 8, v66
	s_and_saveexec_b64 s[8:9], vcc
	s_cbranch_execz .LBB0_3710
	v_lshrrev_b64 v[68:69], v71, s[6:7]
	v_lshl_add_u32 v66, v72, 2, 0
	s_mov_b32 s0, 0
	s_mov_b64 s[6:7], exec
	ds_write_b32 v66, v68 offset:16384

.LBB0_3711:
	v_add_u32_e32 v78, s2, v68
	ds_read2_b32 v[198:199], v78 offset1:1
	ds_read2_b32 v[200:201], v78 offset0:2 offset1:3
	ds_read2_b32 v[202:203], v78 offset0:4 offset1:5
	ds_read2_b32 v[204:205], v78 offset0:6 offset1:7
	ds_read2_b32 v[206:207], v78 offset0:8 offset1:9
	ds_read2_b32 v[208:209], v78 offset0:10 offset1:11
	ds_read2_b32 v[210:211], v78 offset0:12 offset1:13
	ds_read2_b32 v[212:213], v78 offset0:14 offset1:15
	v_cmp_lt_u32_e64 s[14:15], s3, v84
	v_cmp_lt_u32_e64 s[16:17], s0, v67
	s_add_i32 s2, s2, 64
	s_waitcnt lgkmcnt(7)
	v_cmp_gt_f32_e64 s[6:7], v199, v69
	v_cmp_gt_f32_e64 s[8:9], v198, v66
	v_cmp_eq_f32_e64 s[10:11], v198, v66
	v_cmp_eq_f32_e64 s[12:13], v199, v69
	s_and_b64 s[12:13], s[12:13], s[16:17]
	s_and_b64 s[10:11], s[10:11], s[14:15]
	s_add_i32 s16, s3, 2
	s_add_i32 s14, s0, 2
	s_or_b64 s[8:9], s[8:9], s[10:11]
	s_or_b64 s[6:7], s[6:7], s[12:13]
	s_waitcnt lgkmcnt(6)
	v_cmp_eq_f32_e64 s[10:11], v201, v69
	v_cmp_eq_f32_e64 s[12:13], v200, v66
	v_cmp_lt_u32_e64 s[14:15], s14, v67
	v_cmp_lt_u32_e64 s[16:17], s16, v84
	v_cndmask_b32_e64 v75, 0, 1, s[6:7]
	v_cndmask_b32_e64 v79, 0, 1, s[8:9]
	v_cmp_gt_f32_e64 s[6:7], v200, v66
	v_cmp_gt_f32_e64 s[8:9], v201, v69
	s_and_b64 s[12:13], s[12:13], s[16:17]
	s_and_b64 s[10:11], s[10:11], s[14:15]
	s_or_b64 s[8:9], s[8:9], s[10:11]
	s_or_b64 s[6:7], s[6:7], s[12:13]
	v_addc_co_u32_e64 v76, s[6:7], v74, v79, s[6:7]
	v_addc_co_u32_e64 v73, s[6:7], v73, v75, s[8:9]
	s_add_i32 s16, s3, 4
	s_add_i32 s14, s0, 4
	v_cmp_lt_u32_e64 s[14:15], s14, v67
	v_cmp_lt_u32_e64 s[16:17], s16, v84
	s_waitcnt lgkmcnt(5)
	v_cmp_gt_f32_e64 s[6:7], v202, v66
	v_cmp_gt_f32_e64 s[8:9], v203, v69
	v_cmp_eq_f32_e64 s[10:11], v203, v69
	v_cmp_eq_f32_e64 s[12:13], v202, v66
	s_and_b64 s[12:13], s[12:13], s[16:17]
	s_and_b64 s[10:11], s[10:11], s[14:15]
	s_or_b64 s[8:9], s[8:9], s[10:11]
	s_or_b64 s[6:7], s[6:7], s[12:13]
	v_cndmask_b32_e64 v77, 0, 1, s[6:7]
	v_cndmask_b32_e64 v79, 0, 1, s[8:9]
	s_add_i32 s16, s0, 6
	s_add_i32 s14, s3, 6
	s_waitcnt lgkmcnt(4)
	v_cmp_gt_f32_e64 s[6:7], v205, v69
	v_cmp_gt_f32_e64 s[8:9], v204, v66
	v_cmp_eq_f32_e64 s[10:11], v204, v66
	v_cmp_eq_f32_e64 s[12:13], v205, v69
	v_cmp_lt_u32_e64 s[14:15], s14, v84
	v_cmp_lt_u32_e64 s[16:17], s16, v67
	s_and_b64 s[12:13], s[12:13], s[16:17]
	s_and_b64 s[10:11], s[10:11], s[14:15]
	s_or_b64 s[8:9], s[8:9], s[10:11]
	s_or_b64 s[6:7], s[6:7], s[12:13]
	v_addc_co_u32_e64 v73, s[6:7], v73, v79, s[6:7]
	v_addc_co_u32_e64 v76, s[6:7], v76, v77, s[8:9]
	s_waitcnt lgkmcnt(3)
	v_cmp_gt_f32_e64 s[6:7], v207, v69
	v_cmp_gt_f32_e64 s[8:9], v206, v66
	v_cmp_eq_f32_e64 s[10:11], v206, v66
	v_cmp_eq_f32_e64 s[12:13], v207, v69
	s_add_i32 s16, s0, 8
	s_add_i32 s14, s3, 8
	v_cmp_lt_u32_e64 s[14:15], s14, v84
	v_cmp_lt_u32_e64 s[16:17], s16, v67
	s_and_b64 s[12:13], s[12:13], s[16:17]
	s_and_b64 s[10:11], s[10:11], s[14:15]
	s_or_b64 s[8:9], s[8:9], s[10:11]
	s_or_b64 s[6:7], s[6:7], s[12:13]
	v_cndmask_b32_e64 v77, 0, 1, s[6:7]
	v_cndmask_b32_e64 v79, 0, 1, s[8:9]
	s_add_i32 s16, s3, 10
	s_add_i32 s14, s0, 10
	s_waitcnt lgkmcnt(2)
	v_cmp_gt_f32_e64 s[6:7], v208, v66
	v_cmp_gt_f32_e64 s[8:9], v209, v69
	v_cmp_eq_f32_e64 s[10:11], v209, v69
	v_cmp_eq_f32_e64 s[12:13], v208, v66
	v_cmp_lt_u32_e64 s[14:15], s14, v67
	v_cmp_lt_u32_e64 s[16:17], s16, v84
	s_and_b64 s[12:13], s[12:13], s[16:17]
	s_and_b64 s[10:11], s[10:11], s[14:15]
	s_or_b64 s[8:9], s[8:9], s[10:11]
	s_or_b64 s[6:7], s[6:7], s[12:13]
	v_addc_co_u32_e64 v76, s[6:7], v76, v79, s[6:7]
	v_addc_co_u32_e64 v73, s[6:7], v73, v77, s[8:9]
	s_waitcnt lgkmcnt(1)
	v_cmp_gt_f32_e64 s[6:7], v210, v66
	v_cmp_gt_f32_e64 s[8:9], v211, v69
	v_cmp_eq_f32_e64 s[10:11], v211, v69
	v_cmp_eq_f32_e64 s[12:13], v210, v66
	s_add_i32 s16, s3, 12
	s_add_i32 s14, s0, 12
	v_cmp_lt_u32_e64 s[14:15], s14, v67
	v_cmp_lt_u32_e64 s[16:17], s16, v84
	s_and_b64 s[12:13], s[12:13], s[16:17]
	s_and_b64 s[10:11], s[10:11], s[14:15]
	s_add_i32 s16, s0, 14
	s_add_i32 s14, s3, 14
	s_or_b64 s[8:9], s[8:9], s[10:11]
	s_or_b64 s[6:7], s[6:7], s[12:13]
	s_waitcnt lgkmcnt(0)
	v_cmp_eq_f32_e64 s[10:11], v212, v66
	v_cmp_eq_f32_e64 s[12:13], v213, v69
	v_cmp_lt_u32_e64 s[14:15], s14, v84
	v_cmp_lt_u32_e64 s[16:17], s16, v67
	v_cndmask_b32_e64 v77, 0, 1, s[6:7]
	v_cndmask_b32_e64 v79, 0, 1, s[8:9]
	v_cmp_gt_f32_e64 s[6:7], v213, v69
	v_cmp_gt_f32_e64 s[8:9], v212, v66
	s_and_b64 s[12:13], s[12:13], s[16:17]
	s_and_b64 s[10:11], s[10:11], s[14:15]
	s_or_b64 s[8:9], s[8:9], s[10:11]
	s_or_b64 s[6:7], s[6:7], s[12:13]
	s_add_i32 s3, s3, 16
	s_add_i32 s0, s0, 16
	v_addc_co_u32_e64 v73, s[6:7], v73, v79, s[6:7]
	v_addc_co_u32_e64 v74, s[6:7], v76, v77, s[8:9]
	s_cmpk_lg_i32 s2, 0x80
	s_cbranch_scc1 .LBB0_3711
	v_add_u32_e32 v66, v74, v73
	v_cmp_gt_u32_e64 s[6:7], 8, v66
	s_and_saveexec_b64 s[8:9], vcc
	s_cbranch_execz .LBB0_3717
	v_lshrrev_b64 v[68:69], v71, s[6:7]
	v_lshl_add_u32 v66, v72, 2, 0
	s_mov_b32 s0, 0
	s_mov_b64 s[6:7], exec
	ds_write_b32 v66, v68 offset:16384

.LBB0_3725:
	v_add_u32_e32 v76, s2, v70
	ds_read2_b32 v[198:199], v76 offset1:1
	ds_read2_b32 v[200:201], v76 offset0:2 offset1:3
	ds_read2_b32 v[202:203], v76 offset0:4 offset1:5
	ds_read2_b32 v[204:205], v76 offset0:6 offset1:7
	ds_read2_b32 v[206:207], v76 offset0:8 offset1:9
	ds_read2_b32 v[208:209], v76 offset0:10 offset1:11
	ds_read2_b32 v[210:211], v76 offset0:12 offset1:13
	ds_read2_b32 v[212:213], v76 offset0:14 offset1:15
	v_cmp_lt_u32_e64 s[14:15], s3, v84
	v_cmp_lt_u32_e64 s[16:17], s0, v67
	s_add_i32 s2, s2, 64
	s_waitcnt lgkmcnt(7)
	v_cmp_gt_f32_e64 s[6:7], v199, v69
	v_cmp_gt_f32_e64 s[8:9], v198, v66
	v_cmp_eq_f32_e64 s[10:11], v198, v66
	v_cmp_eq_f32_e64 s[12:13], v199, v69
	s_and_b64 s[12:13], s[12:13], s[16:17]
	s_and_b64 s[10:11], s[10:11], s[14:15]
	s_add_i32 s16, s3, 2
	s_add_i32 s14, s0, 2
	s_or_b64 s[8:9], s[8:9], s[10:11]
	s_or_b64 s[6:7], s[6:7], s[12:13]
	s_waitcnt lgkmcnt(6)
	v_cmp_eq_f32_e64 s[10:11], v201, v69
	v_cmp_eq_f32_e64 s[12:13], v200, v66
	v_cmp_lt_u32_e64 s[14:15], s14, v67
	v_cmp_lt_u32_e64 s[16:17], s16, v84
	v_cndmask_b32_e64 v77, 0, 1, s[6:7]
	v_cndmask_b32_e64 v78, 0, 1, s[8:9]
	v_cmp_gt_f32_e64 s[6:7], v200, v66
	v_cmp_gt_f32_e64 s[8:9], v201, v69
	s_and_b64 s[12:13], s[12:13], s[16:17]
	s_and_b64 s[10:11], s[10:11], s[14:15]
	s_or_b64 s[8:9], s[8:9], s[10:11]
	s_or_b64 s[6:7], s[6:7], s[12:13]
	v_addc_co_u32_e64 v74, s[6:7], v73, v78, s[6:7]
	v_addc_co_u32_e64 v75, s[6:7], v72, v77, s[8:9]
	s_add_i32 s16, s3, 4
	s_add_i32 s14, s0, 4
	v_cmp_lt_u32_e64 s[14:15], s14, v67
	v_cmp_lt_u32_e64 s[16:17], s16, v84
	s_waitcnt lgkmcnt(5)
	v_cmp_gt_f32_e64 s[6:7], v202, v66
	v_cmp_gt_f32_e64 s[8:9], v203, v69
	v_cmp_eq_f32_e64 s[10:11], v203, v69
	v_cmp_eq_f32_e64 s[12:13], v202, v66
	s_and_b64 s[12:13], s[12:13], s[16:17]
	s_and_b64 s[10:11], s[10:11], s[14:15]
	s_or_b64 s[8:9], s[8:9], s[10:11]
	s_or_b64 s[6:7], s[6:7], s[12:13]
	v_cndmask_b32_e64 v77, 0, 1, s[6:7]
	v_cndmask_b32_e64 v78, 0, 1, s[8:9]
	s_add_i32 s16, s0, 6
	s_add_i32 s14, s3, 6
	s_waitcnt lgkmcnt(4)
	v_cmp_gt_f32_e64 s[6:7], v205, v69
	v_cmp_gt_f32_e64 s[8:9], v204, v66
	v_cmp_eq_f32_e64 s[10:11], v204, v66
	v_cmp_eq_f32_e64 s[12:13], v205, v69
	v_cmp_lt_u32_e64 s[14:15], s14, v84
	v_cmp_lt_u32_e64 s[16:17], s16, v67
	s_and_b64 s[12:13], s[12:13], s[16:17]
	s_and_b64 s[10:11], s[10:11], s[14:15]
	s_or_b64 s[8:9], s[8:9], s[10:11]
	s_or_b64 s[6:7], s[6:7], s[12:13]
	v_addc_co_u32_e64 v75, s[6:7], v75, v78, s[6:7]
	v_addc_co_u32_e64 v74, s[6:7], v74, v77, s[8:9]
	s_waitcnt lgkmcnt(3)
	v_cmp_gt_f32_e64 s[6:7], v207, v69
	v_cmp_gt_f32_e64 s[8:9], v206, v66
	v_cmp_eq_f32_e64 s[10:11], v206, v66
	v_cmp_eq_f32_e64 s[12:13], v207, v69
	s_add_i32 s16, s0, 8
	s_add_i32 s14, s3, 8
	v_cmp_lt_u32_e64 s[14:15], s14, v84
	v_cmp_lt_u32_e64 s[16:17], s16, v67
	s_and_b64 s[12:13], s[12:13], s[16:17]
	s_and_b64 s[10:11], s[10:11], s[14:15]
	s_or_b64 s[8:9], s[8:9], s[10:11]
	s_or_b64 s[6:7], s[6:7], s[12:13]
	v_cndmask_b32_e64 v77, 0, 1, s[6:7]
	v_cndmask_b32_e64 v78, 0, 1, s[8:9]
	s_add_i32 s16, s3, 10
	s_add_i32 s14, s0, 10
	s_waitcnt lgkmcnt(2)
	v_cmp_gt_f32_e64 s[6:7], v208, v66
	v_cmp_gt_f32_e64 s[8:9], v209, v69
	v_cmp_eq_f32_e64 s[10:11], v209, v69
	v_cmp_eq_f32_e64 s[12:13], v208, v66
	v_cmp_lt_u32_e64 s[14:15], s14, v67
	v_cmp_lt_u32_e64 s[16:17], s16, v84
	s_and_b64 s[12:13], s[12:13], s[16:17]
	s_and_b64 s[10:11], s[10:11], s[14:15]
	s_or_b64 s[8:9], s[8:9], s[10:11]
	s_or_b64 s[6:7], s[6:7], s[12:13]
	v_addc_co_u32_e64 v74, s[6:7], v74, v78, s[6:7]
	v_addc_co_u32_e64 v75, s[6:7], v75, v77, s[8:9]
	s_waitcnt lgkmcnt(1)
	v_cmp_gt_f32_e64 s[6:7], v210, v66
	v_cmp_gt_f32_e64 s[8:9], v211, v69
	v_cmp_eq_f32_e64 s[10:11], v211, v69
	v_cmp_eq_f32_e64 s[12:13], v210, v66
	s_add_i32 s16, s3, 12
	s_add_i32 s14, s0, 12
	v_cmp_lt_u32_e64 s[14:15], s14, v67
	v_cmp_lt_u32_e64 s[16:17], s16, v84
	s_and_b64 s[12:13], s[12:13], s[16:17]
	s_and_b64 s[10:11], s[10:11], s[14:15]
	s_add_i32 s16, s0, 14
	s_add_i32 s14, s3, 14
	s_or_b64 s[8:9], s[8:9], s[10:11]
	s_or_b64 s[6:7], s[6:7], s[12:13]
	s_waitcnt lgkmcnt(0)
	v_cmp_eq_f32_e64 s[10:11], v212, v66
	v_cmp_eq_f32_e64 s[12:13], v213, v69
	v_cmp_lt_u32_e64 s[14:15], s14, v84
	v_cmp_lt_u32_e64 s[16:17], s16, v67
	v_cndmask_b32_e64 v77, 0, 1, s[6:7]
	v_cndmask_b32_e64 v78, 0, 1, s[8:9]
	v_cmp_gt_f32_e64 s[6:7], v213, v69
	v_cmp_gt_f32_e64 s[8:9], v212, v66
	s_and_b64 s[12:13], s[12:13], s[16:17]
	s_and_b64 s[10:11], s[10:11], s[14:15]
	s_or_b64 s[8:9], s[8:9], s[10:11]
	s_or_b64 s[6:7], s[6:7], s[12:13]
	s_add_i32 s3, s3, 16
	s_add_i32 s0, s0, 16
	v_addc_co_u32_e64 v72, s[6:7], v75, v78, s[6:7]
	v_addc_co_u32_e64 v73, s[6:7], v74, v77, s[8:9]
	s_cmpk_lg_i32 s2, 0x80
	s_cbranch_scc1 .LBB0_3725
	v_add_u32_e32 v66, v73, v72
	v_cmp_gt_u32_e64 s[6:7], 8, v66
	s_and_saveexec_b64 s[8:9], vcc
	s_cbranch_execz .LBB0_3731
	v_lshrrev_b64 v[66:67], v71, s[6:7]
	v_lshl_add_u32 v67, v68, 2, 0
	s_mov_b32 s0, 0
	s_mov_b64 s[6:7], exec
	ds_write_b32 v67, v66 offset:16384

.LBB0_3959:
	s_lshl_b32 s0, s20, 8
	v_mov_b32_e32 v2, v247
	v_mov_b32_e32 v3, v246
	s_or_b32 s0, s0, s44
	s_lshl_b32 s20, s20, 2
	v_lshl_add_u32 v26, v2, 3, s0
	s_lshl_b32 s0, s50, 8
	s_add_i32 s0, s0, s43
	v_add_u32_e32 v28, s0, v3
	v_ashrrev_i32_e32 v27, 31, v26
	v_lshlrev_b64 v[52:53], 1, v[26:27]
	v_ashrrev_i32_e32 v29, 31, v28
	v_add_u32_e32 v40, 16, v28
	v_lshl_add_u64 v[30:31], s[8:9], 0, v[52:53]
	v_lshlrev_b64 v[54:55], 12, v[28:29]
	v_ashrrev_i32_e32 v41, 31, v40
	v_add_u32_e32 v36, 32, v28
	v_cmp_eq_u32_e32 vcc, 0, v2
	v_lshl_add_u64 v[2:3], v[30:31], 0, v[54:55]
	v_lshlrev_b64 v[42:43], 12, v[40:41]
	v_ashrrev_i32_e32 v37, 31, v36
	v_add_u32_e32 v32, 48, v28
	global_load_dwordx4 v[44:47], v[2:3], off
	global_load_dwordx4 v[48:51], v[2:3], off offset:256
	v_lshl_add_u64 v[2:3], v[30:31], 0, v[42:43]
	v_lshlrev_b64 v[38:39], 12, v[36:37]
	v_ashrrev_i32_e32 v33, 31, v32
	global_load_dwordx4 v[22:25], v[2:3], off
	global_load_dwordx4 v[18:21], v[2:3], off offset:256
	v_lshl_add_u64 v[2:3], v[30:31], 0, v[38:39]
	v_lshlrev_b64 v[34:35], 12, v[32:33]
	global_load_dwordx4 v[14:17], v[2:3], off
	global_load_dwordx4 v[10:13], v[2:3], off offset:256
	v_lshl_add_u64 v[2:3], v[30:31], 0, v[34:35]
	global_load_dwordx4 v[6:9], v[2:3], off
	s_nop 0
	global_load_dwordx4 v[2:5], v[2:3], off offset:256
	v_lshl_add_u64 v[54:55], s[8:9], 0, v[54:55]
	v_lshl_add_u64 v[52:53], v[54:55], 0, v[52:53]
	s_ashr_i32 s21, s20, 31
	s_waitcnt vmcnt(0)
	s_nop 0
	v_and_b32_e32 v57, 0xffff0000, v44
	v_lshlrev_b32_e32 v56, 16, v44
	v_and_b32_e32 v59, 0xffff0000, v45
	v_lshlrev_b32_e32 v58, 16, v45
	v_and_b32_e32 v45, 0xffff0000, v46
	v_lshlrev_b32_e32 v44, 16, v46
	v_and_b32_e32 v61, 0xffff0000, v47
	v_lshlrev_b32_e32 v60, 16, v47
	v_pk_fma_f32 v[58:59], v[192:193], s[78:79], v[58:59] op_sel_hi:[1,0,1]
	v_pk_fma_f32 v[56:57], v[190:191], s[78:79], v[56:57] op_sel_hi:[1,0,1]
	v_pk_fma_f32 v[60:61], v[188:189], s[78:79], v[60:61] op_sel_hi:[1,0,1]
	v_pk_fma_f32 v[62:63], v[186:187], s[78:79], v[44:45] op_sel_hi:[1,0,1]
	v_cvt_pk_bf16_f32 v44, v56, v57
	v_cvt_pk_bf16_f32 v45, v58, v59
	v_cvt_pk_bf16_f32 v46, v62, v63
	v_cvt_pk_bf16_f32 v47, v60, v61
	global_store_dwordx4 v[52:53], v[44:47], off
	s_nop 1
	v_mul_f32_e32 v44, v57, v57
	v_mul_f32_e32 v45, v59, v59
	v_fmac_f32_e32 v44, v56, v56
	v_fmac_f32_e32 v45, v58, v58
	v_add_f32_e32 v44, v44, v45
	v_mul_f32_e32 v45, v63, v63
	v_mul_f32_e32 v46, v61, v61
	v_fmac_f32_e32 v45, v62, v62
	v_fmac_f32_e32 v46, v60, v60
	v_add_f32_e32 v45, v45, v46
	v_add_f32_e32 v58, v44, v45
	v_and_b32_e32 v45, 0xffff0000, v48
	v_lshlrev_b32_e32 v44, 16, v48
	v_and_b32_e32 v47, 0xffff0000, v49
	v_lshlrev_b32_e32 v46, 16, v49
	v_pk_fma_f32 v[48:49], v[184:185], s[78:79], v[46:47] op_sel_hi:[1,0,1]
	v_pk_fma_f32 v[54:55], v[182:183], s[78:79], v[44:45] op_sel_hi:[1,0,1]
	v_and_b32_e32 v45, 0xffff0000, v50
	v_lshlrev_b32_e32 v44, 16, v50
	v_and_b32_e32 v47, 0xffff0000, v51
	v_lshlrev_b32_e32 v46, 16, v51
	v_pk_fma_f32 v[50:51], v[180:181], s[78:79], v[46:47] op_sel_hi:[1,0,1]
	v_pk_fma_f32 v[56:57], v[178:179], s[78:79], v[44:45] op_sel_hi:[1,0,1]
	v_cvt_pk_bf16_f32 v44, v54, v55
	v_cvt_pk_bf16_f32 v45, v48, v49
	v_cvt_pk_bf16_f32 v46, v56, v57
	v_cvt_pk_bf16_f32 v47, v50, v51
	global_store_dwordx4 v[52:53], v[44:47], off offset:256
	v_add_u32_e32 v186, 0x80, v28
	v_ashrrev_i32_e32 v187, 31, v186
	v_lshlrev_b64 v[186:187], 12, v[186:187]
	v_lshl_add_u64 v[186:187], v[30:31], 0, v[186:187]
	global_load_dwordx4 v[178:181], v[186:187], off
	global_load_dwordx4 v[182:185], v[186:187], off offset:256
	s_nop 1
	v_mul_f32_e32 v44, v55, v55
	v_mul_f32_e32 v45, v49, v49
	v_fmac_f32_e32 v44, v54, v54
	v_fmac_f32_e32 v45, v48, v48
	v_add_f32_e32 v44, v44, v45
	v_mul_f32_e32 v45, v57, v57
	v_mul_f32_e32 v46, v51, v51
	v_fmac_f32_e32 v45, v56, v56
	v_fmac_f32_e32 v46, v50, v50
	v_add_f32_e32 v45, v45, v46
	v_add_f32_e32 v44, v44, v45
	v_add_f32_e32 v44, v58, v44
	ds_bpermute_b32 v45, v249, v44
	s_waitcnt lgkmcnt(0)
	v_add_f32_e32 v44, v44, v45
	ds_bpermute_b32 v45, v250, v44
	s_and_saveexec_b64 s[22:23], vcc
	s_cbranch_execz .LBB0_3961
	v_lshlrev_b64 v[46:47], 7, v[28:29]
	v_lshl_add_u64 v[46:47], s[10:11], 0, v[46:47]
	v_lshl_add_u64 v[46:47], s[20:21], 2, v[46:47]
	s_lshl_b32 s92, s42, 2
	v_lshl_add_u64 v[46:47], v[46:47], 0, s[92:93]
	s_waitcnt lgkmcnt(0)
	v_add_f32_e32 v29, v44, v45
	global_store_dword v[46:47], v29, off
.LBB0_3961:
	s_or_b64 exec, exec, s[22:23]
	s_waitcnt lgkmcnt(0)
	v_and_b32_e32 v45, 0xffff0000, v22
	v_lshlrev_b32_e32 v44, 16, v22
	v_and_b32_e32 v47, 0xffff0000, v23
	v_lshlrev_b32_e32 v46, 16, v23
	v_pk_fma_f32 v[44:45], v[174:175], s[78:79], v[44:45] op_sel_hi:[1,0,1]
	v_pk_fma_f32 v[46:47], v[176:177], s[78:79], v[46:47] op_sel_hi:[1,0,1]
	v_and_b32_e32 v23, 0xffff0000, v24
	v_lshlrev_b32_e32 v22, 16, v24
	v_mul_f32_e32 v29, v45, v45
	v_and_b32_e32 v49, 0xffff0000, v25
	v_lshlrev_b32_e32 v48, 16, v25
	v_pk_fma_f32 v[50:51], v[170:171], s[78:79], v[22:23] op_sel_hi:[1,0,1]
	v_cvt_pk_bf16_f32 v22, v44, v45
	v_fmac_f32_e32 v29, v44, v44
	v_mul_f32_e32 v44, v47, v47
	v_pk_fma_f32 v[48:49], v[172:173], s[78:79], v[48:49] op_sel_hi:[1,0,1]
	v_fmac_f32_e32 v44, v46, v46
	v_add_f32_e32 v29, v29, v44
	v_mul_f32_e32 v44, v51, v51
	v_mul_f32_e32 v45, v49, v49
	v_fmac_f32_e32 v44, v50, v50
	v_fmac_f32_e32 v45, v48, v48
	v_add_f32_e32 v44, v44, v45
	v_cvt_pk_bf16_f32 v23, v46, v47
	v_add_f32_e32 v29, v29, v44
	v_and_b32_e32 v45, 0xffff0000, v18
	v_and_b32_e32 v47, 0xffff0000, v19
	v_lshlrev_b32_e32 v44, 16, v18
	v_lshlrev_b32_e32 v46, 16, v19
	v_pk_fma_f32 v[46:47], v[168:169], s[78:79], v[46:47] op_sel_hi:[1,0,1]
	v_pk_fma_f32 v[18:19], v[166:167], s[78:79], v[44:45] op_sel_hi:[1,0,1]
	v_cvt_pk_bf16_f32 v25, v48, v49
	v_and_b32_e32 v45, 0xffff0000, v20
	v_and_b32_e32 v49, 0xffff0000, v21
	v_lshlrev_b32_e32 v44, 16, v20
	v_lshlrev_b32_e32 v48, 16, v21
	v_mul_f32_e32 v20, v19, v19
	v_mul_f32_e32 v21, v47, v47
	v_pk_fma_f32 v[48:49], v[164:165], s[78:79], v[48:49] op_sel_hi:[1,0,1]
	v_pk_fma_f32 v[44:45], v[162:163], s[78:79], v[44:45] op_sel_hi:[1,0,1]
	v_fmac_f32_e32 v20, v18, v18
	v_fmac_f32_e32 v21, v46, v46
	v_cvt_pk_bf16_f32 v24, v50, v51
	v_add_f32_e32 v20, v20, v21
	v_mul_f32_e32 v21, v45, v45
	v_mul_f32_e32 v50, v49, v49
	v_fmac_f32_e32 v21, v44, v44
	v_fmac_f32_e32 v50, v48, v48
	v_add_f32_e32 v21, v21, v50
	v_add_f32_e32 v20, v20, v21
	v_add_f32_e32 v29, v29, v20
	ds_bpermute_b32 v50, v249, v29
	v_lshl_add_u64 v[20:21], s[8:9], 0, v[42:43]
	v_lshl_add_u64 v[42:43], v[26:27], 1, v[20:21]
	v_cvt_pk_bf16_f32 v20, v18, v19
	global_store_dwordx4 v[42:43], v[22:25], off
	s_waitcnt lgkmcnt(0)
	v_add_f32_e32 v18, v29, v50
	ds_bpermute_b32 v19, v250, v18
	v_cvt_pk_bf16_f32 v21, v46, v47
	v_cvt_pk_bf16_f32 v22, v44, v45
	v_cvt_pk_bf16_f32 v23, v48, v49
	global_store_dwordx4 v[42:43], v[20:23], off offset:256
	v_add_u32_e32 v186, 0x90, v28
	v_ashrrev_i32_e32 v187, 31, v186
	v_lshlrev_b64 v[186:187], 12, v[186:187]
	v_lshl_add_u64 v[186:187], v[30:31], 0, v[186:187]
	global_load_dwordx4 v[162:165], v[186:187], off
	global_load_dwordx4 v[166:169], v[186:187], off offset:256
	v_add_u32_e32 v188, 0xa0, v28
	v_ashrrev_i32_e32 v189, 31, v188
	v_lshlrev_b64 v[188:189], 12, v[188:189]
	v_lshl_add_u64 v[188:189], v[30:31], 0, v[188:189]
	global_load_dwordx4 v[170:173], v[188:189], off
	global_load_dwordx4 v[174:177], v[188:189], off offset:256
	s_and_saveexec_b64 s[22:23], vcc
	s_cbranch_execz .LBB0_3963
	v_lshlrev_b64 v[20:21], 7, v[40:41]
	v_lshl_add_u64 v[20:21], s[10:11], 0, v[20:21]
	v_lshl_add_u64 v[20:21], s[20:21], 2, v[20:21]
	s_lshl_b32 s92, s42, 2
	v_lshl_add_u64 v[20:21], v[20:21], 0, s[92:93]
	s_waitcnt lgkmcnt(0)
	v_add_f32_e32 v18, v18, v19
	global_store_dword v[20:21], v18, off
.LBB0_3963:
	s_or_b64 exec, exec, s[22:23]
	s_waitcnt lgkmcnt(0)
	v_and_b32_e32 v19, 0xffff0000, v14
	v_lshlrev_b32_e32 v18, 16, v14
	v_and_b32_e32 v21, 0xffff0000, v15
	v_lshlrev_b32_e32 v20, 16, v15
	v_pk_fma_f32 v[18:19], v[158:159], s[78:79], v[18:19] op_sel_hi:[1,0,1]
	v_and_b32_e32 v15, 0xffff0000, v16
	v_lshlrev_b32_e32 v14, 16, v16
	v_pk_fma_f32 v[20:21], v[160:161], s[78:79], v[20:21] op_sel_hi:[1,0,1]
	v_pk_fma_f32 v[24:25], v[154:155], s[78:79], v[14:15] op_sel_hi:[1,0,1]
	v_cvt_pk_bf16_f32 v14, v18, v19
	v_mul_f32_e32 v19, v19, v19
	v_and_b32_e32 v23, 0xffff0000, v17
	v_lshlrev_b32_e32 v22, 16, v17
	v_fmac_f32_e32 v19, v18, v18
	v_mul_f32_e32 v18, v21, v21
	v_pk_fma_f32 v[22:23], v[156:157], s[78:79], v[22:23] op_sel_hi:[1,0,1]
	v_fmac_f32_e32 v18, v20, v20
	v_cvt_pk_bf16_f32 v15, v20, v21
	v_add_f32_e32 v18, v19, v18
	v_mul_f32_e32 v19, v25, v25
	v_mul_f32_e32 v20, v23, v23
	v_fmac_f32_e32 v19, v24, v24
	v_fmac_f32_e32 v20, v22, v22
	v_add_f32_e32 v19, v19, v20
	v_cvt_pk_bf16_f32 v16, v24, v25
	v_add_f32_e32 v24, v18, v19
	v_and_b32_e32 v19, 0xffff0000, v10
	v_and_b32_e32 v21, 0xffff0000, v11
	v_lshlrev_b32_e32 v18, 16, v10
	v_lshlrev_b32_e32 v20, 16, v11
	v_pk_fma_f32 v[20:21], v[152:153], s[78:79], v[20:21] op_sel_hi:[1,0,1]
	v_pk_fma_f32 v[10:11], v[150:151], s[78:79], v[18:19] op_sel_hi:[1,0,1]
	v_cvt_pk_bf16_f32 v17, v22, v23
	v_and_b32_e32 v19, 0xffff0000, v12
	v_and_b32_e32 v23, 0xffff0000, v13
	v_lshlrev_b32_e32 v18, 16, v12
	v_lshlrev_b32_e32 v22, 16, v13
	v_mul_f32_e32 v12, v11, v11
	v_mul_f32_e32 v13, v21, v21
	v_pk_fma_f32 v[22:23], v[148:149], s[78:79], v[22:23] op_sel_hi:[1,0,1]
	v_pk_fma_f32 v[18:19], v[146:147], s[78:79], v[18:19] op_sel_hi:[1,0,1]
	v_fmac_f32_e32 v12, v10, v10
	v_fmac_f32_e32 v13, v20, v20
	v_add_f32_e32 v12, v12, v13
	v_mul_f32_e32 v13, v19, v19
	v_mul_f32_e32 v25, v23, v23
	v_fmac_f32_e32 v13, v18, v18
	v_fmac_f32_e32 v25, v22, v22
	v_add_f32_e32 v13, v13, v25
	v_add_f32_e32 v12, v12, v13
	v_add_f32_e32 v29, v24, v12
	ds_bpermute_b32 v40, v249, v29
	v_lshl_add_u64 v[12:13], s[8:9], 0, v[38:39]
	v_lshl_add_u64 v[24:25], v[26:27], 1, v[12:13]
	v_cvt_pk_bf16_f32 v12, v10, v11
	global_store_dwordx4 v[24:25], v[14:17], off
	s_waitcnt lgkmcnt(0)
	v_add_f32_e32 v10, v29, v40
	ds_bpermute_b32 v11, v250, v10
	v_cvt_pk_bf16_f32 v13, v20, v21
	v_cvt_pk_bf16_f32 v14, v18, v19
	v_cvt_pk_bf16_f32 v15, v22, v23
	global_store_dwordx4 v[24:25], v[12:15], off offset:256
	v_add_u32_e32 v186, 0xb0, v28
	v_ashrrev_i32_e32 v187, 31, v186
	v_lshlrev_b64 v[186:187], 12, v[186:187]
	v_lshl_add_u64 v[186:187], v[30:31], 0, v[186:187]
	global_load_dwordx4 v[146:149], v[186:187], off
	global_load_dwordx4 v[150:153], v[186:187], off offset:256
	s_and_saveexec_b64 s[22:23], vcc
	s_cbranch_execz .LBB0_3965
	v_lshlrev_b64 v[12:13], 7, v[36:37]
	v_lshl_add_u64 v[12:13], s[10:11], 0, v[12:13]
	v_lshl_add_u64 v[12:13], s[20:21], 2, v[12:13]
	s_lshl_b32 s92, s42, 2
	v_lshl_add_u64 v[12:13], v[12:13], 0, s[92:93]
	s_waitcnt lgkmcnt(0)
	v_add_f32_e32 v10, v10, v11
	global_store_dword v[12:13], v10, off

.LBB0_3967:
	s_or_b64 exec, exec, s[22:23]
	v_add_u32_e32 v42, 0x80, v28
	v_ashrrev_i32_e32 v43, 31, v42
	v_add_u32_e32 v38, 0x90, v28
	v_lshlrev_b64 v[52:53], 12, v[42:43]
	v_ashrrev_i32_e32 v39, 31, v38
	v_add_u32_e32 v34, 0xa0, v28
	s_waitcnt lgkmcnt(0)
	v_lshl_add_u64 v[2:3], v[30:31], 0, v[52:53]
	v_lshlrev_b64 v[40:41], 12, v[38:39]
	v_ashrrev_i32_e32 v35, 31, v34
	v_add_u32_e32 v28, 0xb0, v28
	v_lshl_add_u64 v[2:3], v[30:31], 0, v[40:41]
	v_lshlrev_b64 v[36:37], 12, v[34:35]
	v_ashrrev_i32_e32 v29, 31, v28
	v_lshl_add_u64 v[2:3], v[30:31], 0, v[36:37]
	v_lshlrev_b64 v[32:33], 12, v[28:29]
	v_lshl_add_u64 v[2:3], v[30:31], 0, v[32:33]
	s_nop 0
	v_lshl_add_u64 v[52:53], s[8:9], 0, v[52:53]
	v_lshl_add_u64 v[52:53], v[26:27], 1, v[52:53]
	s_waitcnt vmcnt(0)
	v_mov_b64_e32 v[44:45], v[178:179]
	v_mov_b64_e32 v[46:47], v[180:181]
	v_mov_b64_e32 v[48:49], v[182:183]
	v_mov_b64_e32 v[50:51], v[184:185]
	v_mov_b64_e32 v[22:23], v[162:163]
	v_mov_b64_e32 v[24:25], v[164:165]
	v_mov_b64_e32 v[18:19], v[166:167]
	v_mov_b64_e32 v[20:21], v[168:169]
	v_mov_b64_e32 v[14:15], v[170:171]
	v_mov_b64_e32 v[16:17], v[172:173]
	v_mov_b64_e32 v[10:11], v[174:175]
	v_mov_b64_e32 v[12:13], v[176:177]
	v_mov_b64_e32 v[6:7], v[146:147]
	v_mov_b64_e32 v[8:9], v[148:149]
	v_mov_b64_e32 v[2:3], v[150:151]
	v_mov_b64_e32 v[4:5], v[152:153]
	s_nop 0
	v_and_b32_e32 v31, 0xffff0000, v44
	v_lshlrev_b32_e32 v30, 16, v44
	v_and_b32_e32 v55, 0xffff0000, v45
	v_lshlrev_b32_e32 v54, 16, v45
	v_pk_fma_f32 v[30:31], v[126:127], s[78:79], v[30:31] op_sel_hi:[1,0,1]
	v_and_b32_e32 v45, 0xffff0000, v46
	v_lshlrev_b32_e32 v44, 16, v46
	v_pk_fma_f32 v[54:55], v[128:129], s[78:79], v[54:55] op_sel_hi:[1,0,1]
	v_and_b32_e32 v57, 0xffff0000, v47
	v_lshlrev_b32_e32 v56, 16, v47
	v_pk_fma_f32 v[58:59], v[122:123], s[78:79], v[44:45] op_sel_hi:[1,0,1]
	v_cvt_pk_bf16_f32 v44, v30, v31
	v_mul_f32_e32 v31, v31, v31
	v_pk_fma_f32 v[56:57], v[124:125], s[78:79], v[56:57] op_sel_hi:[1,0,1]
	v_fmac_f32_e32 v31, v30, v30
	v_mul_f32_e32 v30, v55, v55
	v_cvt_pk_bf16_f32 v45, v54, v55
	v_cvt_pk_bf16_f32 v46, v58, v59
	v_cvt_pk_bf16_f32 v47, v56, v57
	v_fmac_f32_e32 v30, v54, v54
	global_store_dwordx4 v[52:53], v[44:47], off
	v_add_f32_e32 v30, v31, v30
	v_mul_f32_e32 v31, v59, v59
	v_mul_f32_e32 v44, v57, v57
	v_fmac_f32_e32 v31, v58, v58
	v_fmac_f32_e32 v44, v56, v56
	v_add_f32_e32 v31, v31, v44
	v_add_f32_e32 v56, v30, v31
	v_and_b32_e32 v31, 0xffff0000, v48
	v_lshlrev_b32_e32 v30, 16, v48
	v_and_b32_e32 v45, 0xffff0000, v49
	v_lshlrev_b32_e32 v44, 16, v49
	v_pk_fma_f32 v[48:49], v[120:121], s[78:79], v[44:45] op_sel_hi:[1,0,1]
	v_pk_fma_f32 v[30:31], v[118:119], s[78:79], v[30:31] op_sel_hi:[1,0,1]
	v_and_b32_e32 v45, 0xffff0000, v50
	v_lshlrev_b32_e32 v44, 16, v50
	v_and_b32_e32 v47, 0xffff0000, v51
	v_lshlrev_b32_e32 v46, 16, v51
	v_pk_fma_f32 v[54:55], v[114:115], s[78:79], v[44:45] op_sel_hi:[1,0,1]
	v_cvt_pk_bf16_f32 v44, v30, v31
	v_mul_f32_e32 v31, v31, v31
	v_pk_fma_f32 v[50:51], v[116:117], s[78:79], v[46:47] op_sel_hi:[1,0,1]
	v_fmac_f32_e32 v31, v30, v30
	v_mul_f32_e32 v30, v49, v49
	v_cvt_pk_bf16_f32 v45, v48, v49
	v_cvt_pk_bf16_f32 v46, v54, v55
	v_cvt_pk_bf16_f32 v47, v50, v51
	v_fmac_f32_e32 v30, v48, v48
	global_store_dwordx4 v[52:53], v[44:47], off offset:256
	v_add_f32_e32 v30, v31, v30
	v_mul_f32_e32 v31, v55, v55
	v_mul_f32_e32 v44, v51, v51
	v_fmac_f32_e32 v31, v54, v54
	v_fmac_f32_e32 v44, v50, v50
	v_add_f32_e32 v31, v31, v44
	v_add_f32_e32 v30, v30, v31
	v_add_f32_e32 v30, v56, v30
	ds_bpermute_b32 v31, v249, v30
	s_waitcnt lgkmcnt(0)
	v_add_f32_e32 v30, v30, v31
	ds_bpermute_b32 v31, v250, v30
	s_and_saveexec_b64 s[22:23], vcc
	s_cbranch_execz .LBB0_3969
	v_lshlrev_b64 v[42:43], 7, v[42:43]
	v_lshl_add_u64 v[42:43], s[10:11], 0, v[42:43]
	v_lshl_add_u64 v[42:43], s[20:21], 2, v[42:43]
	s_lshl_b32 s92, s42, 2
	v_lshl_add_u64 v[42:43], v[42:43], 0, s[92:93]
	s_waitcnt lgkmcnt(0)
	v_add_f32_e32 v30, v30, v31
	global_store_dword v[42:43], v30, off
